# weight-transpose work queue consumed from both ends (even chunk tickets from the front of the job list, odd tickets from the back)
# speedup vs baseline: 1.0049x; 1.0049x over previous
.LBB0_37:
	s_or_b64 exec, exec, s[10:11]
	v_readfirstlane_b32 s83, v10
	s_cmp_gt_i32 s83, 0x199ff
	s_mov_b64 s[10:11], -1
	s_cbranch_scc1 .LBB0_32
	s_lshr_b32 s8, s83, 2
	s_lshr_b32 s12, s8, 1
	s_bitcmp1_b32 s8, 0
	s_cbranch_scc0 .Lmy_q2e
	s_sub_u32 s12, 0x667f, s12
.Lmy_q2e:
	s_lshl_b32 s83, s12, 2
	s_load_dwordx2 s[10:11], s[28:29], 0x40
	s_lshl_b32 s8, s83, 1
	s_lshl_b32 s84, s83, 2
	s_lshl_b32 s85, s83, 6
	s_add_i32 s86, s8, 0xffff7300
	s_add_i32 s87, s83, 4
	s_branch .LBB0_40
